# phase_final token loop (3 copies): all 16 row loads (h, u, gain) issued together at the loop header next to the ssq load instead of five dependent batches; in-body vm waits removed; on top of v39
# baseline (speedup 1.0000x reference)
.LBB0_2483:
	s_or_b64 exec, exec, s[0:1]
	v_lshl_add_u64 v[2:3], s[4:5], 0, v[16:17]
	v_add_co_u32_e64 v20, s[0:1], s14, v2
	s_waitcnt vmcnt(0)
	ds_bpermute_b32 v27, v1, v18
	v_addc_co_u32_e64 v21, s[0:1], 0, v3, s[0:1]
	v_mov_b32_e32 v28, v140
	v_mov_b32_e32 v29, v141
	v_mov_b32_e32 v30, v142
	v_mov_b32_e32 v31, v143
	v_mov_b32_e32 v32, v144
	v_mov_b32_e32 v33, v145
	v_mov_b32_e32 v34, v146
	v_mov_b32_e32 v35, v147
	v_mov_b32_e32 v36, v148
	v_mov_b32_e32 v37, v149
	v_mov_b32_e32 v38, v150
	v_mov_b32_e32 v39, v151
	v_mov_b32_e32 v2, v152
	v_mov_b32_e32 v3, v153
	v_mov_b32_e32 v4, v154
	v_mov_b32_e32 v5, v155
	v_lshl_add_u64 v[20:21], s[6:7], 0, v[16:17]
	v_add_co_u32_e64 v20, s[0:1], s15, v20
	s_waitcnt lgkmcnt(0)
	v_add_f32_e32 v18, v18, v27
	v_addc_co_u32_e64 v21, s[0:1], 0, v21, s[0:1]
	ds_bpermute_b32 v27, v19, v18
	v_lshl_add_u64 v[52:53], s[4:5], 0, v[6:7]
	s_add_i32 s2, s2, s90
	s_add_u32 s4, s4, s10
	s_addc_u32 s5, s5, s11
	s_waitcnt lgkmcnt(0)
	v_add_f32_e32 v18, v18, v27
	ds_bpermute_b32 v27, v22, v18
	s_add_u32 s6, s6, s12
	s_addc_u32 s7, s7, s13
	s_cmpk_lt_i32 s2, 0x6000
	v_lshl_add_u64 v[14:15], v[14:15], 0, s[8:9]
	s_waitcnt lgkmcnt(0)
	v_add_f32_e32 v18, v18, v27
	ds_bpermute_b32 v27, v23, v18


	v_mov_b32_e32 v40, v156
	v_mov_b32_e32 v41, v157
	v_mov_b32_e32 v42, v158
	v_mov_b32_e32 v43, v159
	v_mov_b32_e32 v44, v172
	v_mov_b32_e32 v45, v173
	v_mov_b32_e32 v46, v174
	v_mov_b32_e32 v47, v175
	v_mov_b32_e32 v48, v176
	v_mov_b32_e32 v49, v177
	v_mov_b32_e32 v50, v178
	v_mov_b32_e32 v51, v179
	s_waitcnt lgkmcnt(0)
	v_add_f32_e32 v18, v18, v27
	ds_bpermute_b32 v27, v24, v18
	v_lshlrev_b32_e32 v54, 16, v28
	v_and_b32_e32 v55, 0xffff0000, v28
	v_lshlrev_b32_e32 v56, 16, v29
	v_and_b32_e32 v57, 0xffff0000, v29
	s_waitcnt lgkmcnt(0)
	v_add_f32_e32 v18, v18, v27
	ds_bpermute_b32 v27, v25, v18
	v_lshlrev_b32_e32 v58, 16, v30
	v_and_b32_e32 v59, 0xffff0000, v30
	v_lshlrev_b32_e32 v60, 16, v31
	v_and_b32_e32 v61, 0xffff0000, v31
	s_waitcnt lgkmcnt(0)
	v_add_f32_e32 v18, v18, v27
	v_fmamk_f32 v18, v18, 0x3a000000, v26
	v_mul_f32_e32 v27, 0x4b800000, v18
	v_cmp_gt_f32_e64 s[0:1], s3, v18

	v_lshlrev_b32_e32 v28, 16, v40
	v_cndmask_b32_e64 v18, v18, v27, s[0:1]
	v_rsq_f32_e32 v18, v18
	v_and_b32_e32 v29, 0xffff0000, v40
	v_lshlrev_b32_e32 v30, 16, v41
	v_and_b32_e32 v31, 0xffff0000, v41
	v_mul_f32_e32 v27, 0x45800000, v18
	v_cndmask_b32_e64 v18, v18, v27, s[0:1]
	v_lshlrev_b32_e32 v40, 16, v42
	v_and_b32_e32 v41, 0xffff0000, v42
	v_lshlrev_b32_e32 v42, 16, v43
	v_and_b32_e32 v43, 0xffff0000, v43
	v_mul_f32_e32 v28, v18, v28
	v_mul_f32_e32 v29, v18, v29
	v_mul_f32_e32 v30, v18, v30
	v_mul_f32_e32 v31, v18, v31
	v_mul_f32_e32 v40, v18, v40
	v_mul_f32_e32 v41, v18, v41
	v_mul_f32_e32 v42, v18, v42
	v_mul_f32_e32 v43, v18, v43

	v_fma_f32 v28, v44, v28, v54
	v_fma_f32 v29, v45, v29, v55
	v_fma_f32 v30, v46, v30, v56
	v_fma_f32 v31, v47, v31, v57

	v_fma_f32 v40, v48, v40, v58
	v_fma_f32 v41, v49, v41, v59
	v_fma_f32 v42, v50, v42, v60
	v_fma_f32 v43, v51, v43, v61
	global_store_dwordx4 v[52:53], v[28:31], off
	global_store_dwordx4 v[52:53], v[40:43], off offset:16
	s_nop 1
	v_mov_b32_e32 v28, v160
	v_mov_b32_e32 v29, v161
	v_mov_b32_e32 v30, v162
	v_mov_b32_e32 v31, v163
	s_nop 0
	v_mov_b32_e32 v40, v180
	v_mov_b32_e32 v41, v181
	v_mov_b32_e32 v42, v182
	v_mov_b32_e32 v43, v183
	v_mov_b32_e32 v44, v184
	v_mov_b32_e32 v45, v185
	v_mov_b32_e32 v46, v186
	v_mov_b32_e32 v47, v187
	v_lshlrev_b32_e32 v48, 16, v32
	v_and_b32_e32 v49, 0xffff0000, v32
	v_lshlrev_b32_e32 v32, 16, v33
	v_and_b32_e32 v33, 0xffff0000, v33
	v_lshlrev_b32_e32 v50, 16, v34
	v_and_b32_e32 v51, 0xffff0000, v34
	v_lshlrev_b32_e32 v34, 16, v35
	v_and_b32_e32 v35, 0xffff0000, v35

	v_lshlrev_b32_e32 v54, 16, v28
	v_and_b32_e32 v55, 0xffff0000, v28
	v_lshlrev_b32_e32 v28, 16, v29
	v_and_b32_e32 v29, 0xffff0000, v29
	v_lshlrev_b32_e32 v56, 16, v30
	v_and_b32_e32 v57, 0xffff0000, v30
	v_lshlrev_b32_e32 v30, 16, v31
	v_and_b32_e32 v31, 0xffff0000, v31
	v_mul_f32_e32 v54, v18, v54
	v_mul_f32_e32 v55, v18, v55
	v_mul_f32_e32 v58, v18, v28
	v_mul_f32_e32 v59, v18, v29
	v_mul_f32_e32 v56, v18, v56
	v_mul_f32_e32 v57, v18, v57
	v_mul_f32_e32 v60, v18, v30
	v_mul_f32_e32 v61, v18, v31

	v_fma_f32 v28, v40, v54, v48
	v_fma_f32 v29, v41, v55, v49
	v_fma_f32 v30, v42, v58, v32
	v_fma_f32 v31, v43, v59, v33

	v_fma_f32 v32, v44, v56, v50
	v_fma_f32 v33, v45, v57, v51
	v_fma_f32 v34, v46, v60, v34
	v_fma_f32 v35, v47, v61, v35
	global_store_dwordx4 v[52:53], v[28:31], off offset:2048
	global_store_dwordx4 v[52:53], v[32:35], off offset:2064
	s_nop 1
	v_mov_b32_e32 v28, v164
	v_mov_b32_e32 v29, v165
	v_mov_b32_e32 v30, v166
	v_mov_b32_e32 v31, v167
	s_nop 0
	v_mov_b32_e32 v32, v188
	v_mov_b32_e32 v33, v189
	v_mov_b32_e32 v34, v190
	v_mov_b32_e32 v35, v191
	v_mov_b32_e32 v40, v192
	v_mov_b32_e32 v41, v193
	v_mov_b32_e32 v42, v194
	v_mov_b32_e32 v43, v195
	v_add_co_u32_e64 v44, s[0:1], s14, v52
	v_lshlrev_b32_e32 v46, 16, v36
	s_nop 0
	v_addc_co_u32_e64 v45, s[0:1], 0, v53, s[0:1]
	v_and_b32_e32 v47, 0xffff0000, v36
	v_lshlrev_b32_e32 v36, 16, v37
	v_and_b32_e32 v37, 0xffff0000, v37
	v_lshlrev_b32_e32 v48, 16, v38
	v_and_b32_e32 v49, 0xffff0000, v38
	v_lshlrev_b32_e32 v38, 16, v39
	v_and_b32_e32 v39, 0xffff0000, v39

	v_lshlrev_b32_e32 v50, 16, v28
	v_and_b32_e32 v51, 0xffff0000, v28
	v_lshlrev_b32_e32 v28, 16, v29
	v_and_b32_e32 v29, 0xffff0000, v29
	v_lshlrev_b32_e32 v52, 16, v30
	v_and_b32_e32 v53, 0xffff0000, v30
	v_lshlrev_b32_e32 v30, 16, v31
	v_and_b32_e32 v31, 0xffff0000, v31
	v_mul_f32_e32 v50, v18, v50
	v_mul_f32_e32 v51, v18, v51
	v_mul_f32_e32 v54, v18, v28
	v_mul_f32_e32 v55, v18, v29
	v_mul_f32_e32 v52, v18, v52
	v_mul_f32_e32 v53, v18, v53
	v_mul_f32_e32 v56, v18, v30
	v_mul_f32_e32 v57, v18, v31

	v_fma_f32 v28, v32, v50, v46
	v_fma_f32 v29, v33, v51, v47
	v_fma_f32 v30, v34, v54, v36
	v_fma_f32 v31, v35, v55, v37

	v_fma_f32 v32, v40, v52, v48
	v_fma_f32 v33, v41, v53, v49
	v_fma_f32 v34, v42, v56, v38
	v_fma_f32 v35, v43, v57, v39
	global_store_dwordx4 v[44:45], v[28:31], off
	global_store_dwordx4 v[44:45], v[32:35], off offset:16
	s_nop 1
	v_mov_b32_e32 v28, v168
	v_mov_b32_e32 v29, v169
	v_mov_b32_e32 v30, v170
	v_mov_b32_e32 v31, v171
	s_nop 0
	v_mov_b32_e32 v32, v196
	v_mov_b32_e32 v33, v197
	v_mov_b32_e32 v34, v198
	v_mov_b32_e32 v35, v199
	v_mov_b32_e32 v36, v200
	v_mov_b32_e32 v37, v201
	v_mov_b32_e32 v38, v202
	v_mov_b32_e32 v39, v203
	v_lshlrev_b32_e32 v20, 16, v2
	v_and_b32_e32 v21, 0xffff0000, v2
	v_lshlrev_b32_e32 v40, 16, v3
	v_and_b32_e32 v41, 0xffff0000, v3
	v_lshlrev_b32_e32 v42, 16, v4
	v_and_b32_e32 v43, 0xffff0000, v4
	v_lshlrev_b32_e32 v46, 16, v5
	v_and_b32_e32 v47, 0xffff0000, v5

	v_lshlrev_b32_e32 v2, 16, v28
	v_and_b32_e32 v3, 0xffff0000, v28
	v_lshlrev_b32_e32 v4, 16, v29
	v_and_b32_e32 v5, 0xffff0000, v29
	v_lshlrev_b32_e32 v28, 16, v30
	v_and_b32_e32 v29, 0xffff0000, v30
	v_lshlrev_b32_e32 v30, 16, v31
	v_and_b32_e32 v31, 0xffff0000, v31
	v_mul_f32_e32 v2, v18, v2
	v_mul_f32_e32 v3, v18, v3
	v_mul_f32_e32 v4, v18, v4
	v_mul_f32_e32 v5, v18, v5
	v_mul_f32_e32 v28, v18, v28
	v_mul_f32_e32 v29, v18, v29
	v_mul_f32_e32 v30, v18, v30
	v_mul_f32_e32 v31, v18, v31

	v_fma_f32 v2, v32, v2, v20
	v_fma_f32 v3, v33, v3, v21
	v_fma_f32 v4, v34, v4, v40
	v_fma_f32 v5, v35, v5, v41

	v_fma_f32 v28, v36, v28, v42
	v_fma_f32 v29, v37, v29, v43
	v_fma_f32 v30, v38, v30, v46
	v_fma_f32 v31, v39, v31, v47
	global_store_dwordx4 v[44:45], v[2:5], off offset:2048
	global_store_dwordx4 v[44:45], v[28:31], off offset:2064
	s_cbranch_scc0 .LBB0_2486
.LBB0_2484:
	v_lshl_add_u64 v[212:213], s[4:5], 0, v[16:17]
	v_lshl_add_u64 v[214:215], s[6:7], 0, v[16:17]
	v_add_co_u32_e64 v212, s[0:1], s14, v212
	s_nop 1
	v_addc_co_u32_e64 v213, s[0:1], 0, v213, s[0:1]
	v_add_co_u32_e64 v214, s[0:1], s15, v214
	s_nop 1
	v_addc_co_u32_e64 v215, s[0:1], 0, v215, s[0:1]
	global_load_dwordx4 v[140:143], v[212:213], off
	global_load_dwordx4 v[144:147], v[212:213], off offset:1024
	global_load_dwordx4 v[148:151], v[212:213], off offset:2048
	global_load_dwordx4 v[152:155], v[212:213], off offset:3072
	global_load_dwordx4 v[156:159], v[214:215], off
	global_load_dwordx4 v[160:163], v[214:215], off offset:1024
	global_load_dwordx4 v[164:167], v[214:215], off offset:2048
	global_load_dwordx4 v[168:171], v[214:215], off offset:3072
	global_load_dwordx4 v[172:175], v[8:9], off
	global_load_dwordx4 v[176:179], v[8:9], off offset:16
	global_load_dwordx4 v[180:183], v[8:9], off offset:2048
	global_load_dwordx4 v[184:187], v[8:9], off offset:2064
	global_load_dwordx4 v[188:191], v[10:11], off
	global_load_dwordx4 v[192:195], v[10:11], off offset:16
	global_load_dwordx4 v[196:199], v[12:13], off
	global_load_dwordx4 v[200:203], v[12:13], off offset:16
	v_mov_b32_e32 v18, 0
	s_and_saveexec_b64 s[0:1], vcc
	s_cbranch_execz .LBB0_2483
	global_load_dword v18, v[14:15], off
	s_branch .LBB0_2483

.LBB0_2600:
	s_or_b64 exec, exec, s[0:1]
	v_lshl_add_u64 v[0:1], s[4:5], 0, v[14:15]
	v_add_co_u32_e64 v18, s[0:1], s14, v0
	s_waitcnt vmcnt(0)
	ds_bpermute_b32 v50, v17, v16
	v_addc_co_u32_e64 v19, s[0:1], 0, v1, s[0:1]
	v_mov_b32_e32 v26, v140
	v_mov_b32_e32 v27, v141
	v_mov_b32_e32 v28, v142
	v_mov_b32_e32 v29, v143
	v_mov_b32_e32 v30, v144
	v_mov_b32_e32 v31, v145
	v_mov_b32_e32 v32, v146
	v_mov_b32_e32 v33, v147
	v_mov_b32_e32 v34, v148
	v_mov_b32_e32 v35, v149
	v_mov_b32_e32 v36, v150
	v_mov_b32_e32 v37, v151
	v_mov_b32_e32 v0, v152
	v_mov_b32_e32 v1, v153
	v_mov_b32_e32 v2, v154
	v_mov_b32_e32 v3, v155
	v_lshl_add_u64 v[18:19], s[6:7], 0, v[14:15]
	v_add_co_u32_e64 v18, s[0:1], s15, v18
	s_waitcnt lgkmcnt(0)
	v_add_f32_e32 v16, v16, v50
	v_addc_co_u32_e64 v19, s[0:1], 0, v19, s[0:1]
	ds_bpermute_b32 v50, v20, v16
	s_add_i32 s2, s2, s90
	v_lshl_add_u64 v[12:13], v[12:13], 0, s[8:9]


	v_mov_b32_e32 v38, v156
	v_mov_b32_e32 v39, v157
	v_mov_b32_e32 v40, v158
	v_mov_b32_e32 v41, v159
	v_mov_b32_e32 v42, v172
	v_mov_b32_e32 v43, v173
	v_mov_b32_e32 v44, v174
	v_mov_b32_e32 v45, v175
	v_mov_b32_e32 v46, v176
	v_mov_b32_e32 v47, v177
	v_mov_b32_e32 v48, v178
	v_mov_b32_e32 v49, v179
	s_waitcnt lgkmcnt(0)
	v_add_f32_e32 v16, v16, v50
	ds_bpermute_b32 v50, v21, v16
	v_and_b32_e32 v53, 0xffff0000, v26
	v_lshlrev_b32_e32 v54, 16, v27
	v_and_b32_e32 v55, 0xffff0000, v27
	v_lshlrev_b32_e32 v56, 16, v28
	s_waitcnt lgkmcnt(0)
	v_add_f32_e32 v16, v16, v50
	ds_bpermute_b32 v50, v22, v16
	v_and_b32_e32 v57, 0xffff0000, v28
	v_lshlrev_b32_e32 v58, 16, v29
	v_and_b32_e32 v59, 0xffff0000, v29
	s_waitcnt lgkmcnt(0)
	v_add_f32_e32 v16, v16, v50
	ds_bpermute_b32 v50, v23, v16
	s_waitcnt lgkmcnt(0)
	v_add_f32_e32 v16, v16, v50
	ds_bpermute_b32 v50, v24, v16
	s_waitcnt lgkmcnt(0)
	v_add_f32_e32 v16, v16, v50
	v_fmamk_f32 v16, v16, 0x3a000000, v25
	v_mul_f32_e32 v50, 0x4b800000, v16
	v_cmp_gt_f32_e64 s[0:1], s3, v16

	v_and_b32_e32 v27, 0xffff0000, v38
	v_cndmask_b32_e64 v16, v16, v50, s[0:1]
	v_rsq_f32_e32 v16, v16
	v_lshlrev_b32_e32 v28, 16, v39
	v_and_b32_e32 v29, 0xffff0000, v39
	v_and_b32_e32 v39, 0xffff0000, v40
	v_mul_f32_e32 v52, 0x45800000, v16
	v_cndmask_b32_e64 v16, v16, v52, s[0:1]
	v_lshlrev_b32_e32 v52, 16, v26
	v_lshlrev_b32_e32 v26, 16, v38
	v_lshlrev_b32_e32 v38, 16, v40
	v_lshlrev_b32_e32 v40, 16, v41
	v_and_b32_e32 v41, 0xffff0000, v41
	v_mul_f32_e32 v26, v16, v26
	v_mul_f32_e32 v27, v16, v27
	v_mul_f32_e32 v28, v16, v28
	v_mul_f32_e32 v29, v16, v29
	v_lshl_add_u64 v[50:51], s[4:5], 0, v[4:5]
	v_mul_f32_e32 v38, v16, v38
	v_mul_f32_e32 v39, v16, v39
	v_mul_f32_e32 v40, v16, v40
	v_mul_f32_e32 v41, v16, v41

	v_fma_f32 v26, v42, v26, v52
	v_fma_f32 v27, v43, v27, v53
	v_fma_f32 v28, v44, v28, v54
	v_fma_f32 v29, v45, v29, v55

	v_fma_f32 v38, v46, v38, v56
	v_fma_f32 v39, v47, v39, v57
	v_fma_f32 v40, v48, v40, v58
	v_fma_f32 v41, v49, v41, v59
	global_store_dwordx4 v[50:51], v[26:29], off
	global_store_dwordx4 v[50:51], v[38:41], off offset:16
	s_nop 1
	v_mov_b32_e32 v26, v160
	v_mov_b32_e32 v27, v161
	v_mov_b32_e32 v28, v162
	v_mov_b32_e32 v29, v163
	s_nop 0
	v_mov_b32_e32 v38, v180
	v_mov_b32_e32 v39, v181
	v_mov_b32_e32 v40, v182
	v_mov_b32_e32 v41, v183
	v_mov_b32_e32 v42, v184
	v_mov_b32_e32 v43, v185
	v_mov_b32_e32 v44, v186
	v_mov_b32_e32 v45, v187
	v_lshlrev_b32_e32 v46, 16, v30
	v_and_b32_e32 v47, 0xffff0000, v30
	v_lshlrev_b32_e32 v30, 16, v31
	v_and_b32_e32 v31, 0xffff0000, v31
	v_lshlrev_b32_e32 v48, 16, v32
	v_and_b32_e32 v49, 0xffff0000, v32
	v_lshlrev_b32_e32 v32, 16, v33
	v_and_b32_e32 v33, 0xffff0000, v33
	s_add_u32 s4, s4, s10
	s_addc_u32 s5, s5, s11
	s_add_u32 s6, s6, s12
	s_addc_u32 s7, s7, s13
	s_cmp_lt_i32 s2, 0x8000

	v_lshlrev_b32_e32 v52, 16, v26
	v_and_b32_e32 v53, 0xffff0000, v26
	v_lshlrev_b32_e32 v26, 16, v27
	v_and_b32_e32 v27, 0xffff0000, v27
	v_lshlrev_b32_e32 v54, 16, v28
	v_and_b32_e32 v55, 0xffff0000, v28
	v_lshlrev_b32_e32 v28, 16, v29
	v_and_b32_e32 v29, 0xffff0000, v29
	v_mul_f32_e32 v52, v16, v52
	v_mul_f32_e32 v53, v16, v53
	v_mul_f32_e32 v56, v16, v26
	v_mul_f32_e32 v57, v16, v27
	v_mul_f32_e32 v54, v16, v54
	v_mul_f32_e32 v55, v16, v55
	v_mul_f32_e32 v58, v16, v28
	v_mul_f32_e32 v59, v16, v29

	v_fma_f32 v26, v38, v52, v46
	v_fma_f32 v27, v39, v53, v47
	v_fma_f32 v28, v40, v56, v30
	v_fma_f32 v29, v41, v57, v31

	v_fma_f32 v30, v42, v54, v48
	v_fma_f32 v31, v43, v55, v49
	v_fma_f32 v32, v44, v58, v32
	v_fma_f32 v33, v45, v59, v33
	global_store_dwordx4 v[50:51], v[26:29], off offset:2048
	global_store_dwordx4 v[50:51], v[30:33], off offset:2064
	s_nop 1
	v_mov_b32_e32 v26, v164
	v_mov_b32_e32 v27, v165
	v_mov_b32_e32 v28, v166
	v_mov_b32_e32 v29, v167
	s_nop 0
	v_mov_b32_e32 v30, v188
	v_mov_b32_e32 v31, v189
	v_mov_b32_e32 v32, v190
	v_mov_b32_e32 v33, v191
	v_mov_b32_e32 v38, v192
	v_mov_b32_e32 v39, v193
	v_mov_b32_e32 v40, v194
	v_mov_b32_e32 v41, v195
	v_add_co_u32_e64 v42, s[0:1], s14, v50
	v_lshlrev_b32_e32 v44, 16, v34
	s_nop 0
	v_addc_co_u32_e64 v43, s[0:1], 0, v51, s[0:1]
	v_and_b32_e32 v45, 0xffff0000, v34
	v_lshlrev_b32_e32 v34, 16, v35
	v_and_b32_e32 v35, 0xffff0000, v35
	v_lshlrev_b32_e32 v46, 16, v36
	v_and_b32_e32 v47, 0xffff0000, v36
	v_lshlrev_b32_e32 v36, 16, v37
	v_and_b32_e32 v37, 0xffff0000, v37

	v_lshlrev_b32_e32 v48, 16, v26
	v_and_b32_e32 v49, 0xffff0000, v26
	v_lshlrev_b32_e32 v26, 16, v27
	v_and_b32_e32 v27, 0xffff0000, v27
	v_lshlrev_b32_e32 v50, 16, v28
	v_and_b32_e32 v51, 0xffff0000, v28
	v_lshlrev_b32_e32 v28, 16, v29
	v_and_b32_e32 v29, 0xffff0000, v29
	v_mul_f32_e32 v48, v16, v48
	v_mul_f32_e32 v49, v16, v49
	v_mul_f32_e32 v52, v16, v26
	v_mul_f32_e32 v53, v16, v27
	v_mul_f32_e32 v50, v16, v50
	v_mul_f32_e32 v51, v16, v51
	v_mul_f32_e32 v54, v16, v28
	v_mul_f32_e32 v55, v16, v29

	v_fma_f32 v26, v30, v48, v44
	v_fma_f32 v27, v31, v49, v45
	v_fma_f32 v28, v32, v52, v34
	v_fma_f32 v29, v33, v53, v35

	v_fma_f32 v30, v38, v50, v46
	v_fma_f32 v31, v39, v51, v47
	v_fma_f32 v32, v40, v54, v36
	v_fma_f32 v33, v41, v55, v37
	global_store_dwordx4 v[42:43], v[26:29], off
	global_store_dwordx4 v[42:43], v[30:33], off offset:16
	s_nop 1
	v_mov_b32_e32 v26, v168
	v_mov_b32_e32 v27, v169
	v_mov_b32_e32 v28, v170
	v_mov_b32_e32 v29, v171
	s_nop 0
	v_mov_b32_e32 v30, v196
	v_mov_b32_e32 v31, v197
	v_mov_b32_e32 v32, v198
	v_mov_b32_e32 v33, v199
	v_mov_b32_e32 v34, v200
	v_mov_b32_e32 v35, v201
	v_mov_b32_e32 v36, v202
	v_mov_b32_e32 v37, v203
	v_lshlrev_b32_e32 v18, 16, v0
	v_and_b32_e32 v19, 0xffff0000, v0
	v_lshlrev_b32_e32 v38, 16, v1
	v_and_b32_e32 v39, 0xffff0000, v1
	v_lshlrev_b32_e32 v40, 16, v2
	v_and_b32_e32 v41, 0xffff0000, v2
	v_lshlrev_b32_e32 v44, 16, v3
	v_and_b32_e32 v45, 0xffff0000, v3

	v_lshlrev_b32_e32 v0, 16, v26
	v_and_b32_e32 v1, 0xffff0000, v26
	v_lshlrev_b32_e32 v2, 16, v27
	v_and_b32_e32 v3, 0xffff0000, v27
	v_lshlrev_b32_e32 v26, 16, v28
	v_and_b32_e32 v27, 0xffff0000, v28
	v_lshlrev_b32_e32 v28, 16, v29
	v_and_b32_e32 v29, 0xffff0000, v29
	v_mul_f32_e32 v0, v16, v0
	v_mul_f32_e32 v1, v16, v1
	v_mul_f32_e32 v2, v16, v2
	v_mul_f32_e32 v3, v16, v3
	v_mul_f32_e32 v26, v16, v26
	v_mul_f32_e32 v27, v16, v27
	v_mul_f32_e32 v28, v16, v28
	v_mul_f32_e32 v29, v16, v29

	v_fma_f32 v0, v30, v0, v18
	v_fma_f32 v1, v31, v1, v19
	v_fma_f32 v2, v32, v2, v38
	v_fma_f32 v3, v33, v3, v39

	v_fma_f32 v26, v34, v26, v40
	v_fma_f32 v27, v35, v27, v41
	v_fma_f32 v28, v36, v28, v44
	v_fma_f32 v29, v37, v29, v45
	global_store_dwordx4 v[42:43], v[0:3], off offset:2048
	global_store_dwordx4 v[42:43], v[26:29], off offset:2064
	s_cbranch_scc0 .LBB0_2603
.LBB0_2601:
	v_lshl_add_u64 v[212:213], s[4:5], 0, v[14:15]
	v_lshl_add_u64 v[214:215], s[6:7], 0, v[14:15]
	v_add_co_u32_e64 v212, s[0:1], s14, v212
	s_nop 1
	v_addc_co_u32_e64 v213, s[0:1], 0, v213, s[0:1]
	v_add_co_u32_e64 v214, s[0:1], s15, v214
	s_nop 1
	v_addc_co_u32_e64 v215, s[0:1], 0, v215, s[0:1]
	global_load_dwordx4 v[140:143], v[212:213], off
	global_load_dwordx4 v[144:147], v[212:213], off offset:1024
	global_load_dwordx4 v[148:151], v[212:213], off offset:2048
	global_load_dwordx4 v[152:155], v[212:213], off offset:3072
	global_load_dwordx4 v[156:159], v[214:215], off
	global_load_dwordx4 v[160:163], v[214:215], off offset:1024
	global_load_dwordx4 v[164:167], v[214:215], off offset:2048
	global_load_dwordx4 v[168:171], v[214:215], off offset:3072
	global_load_dwordx4 v[172:175], v[6:7], off
	global_load_dwordx4 v[176:179], v[6:7], off offset:16
	global_load_dwordx4 v[180:183], v[6:7], off offset:2048
	global_load_dwordx4 v[184:187], v[6:7], off offset:2064
	global_load_dwordx4 v[188:191], v[8:9], off
	global_load_dwordx4 v[192:195], v[8:9], off offset:16
	global_load_dwordx4 v[196:199], v[10:11], off
	global_load_dwordx4 v[200:203], v[10:11], off offset:16
	v_mov_b32_e32 v16, 0
	s_and_saveexec_b64 s[0:1], vcc
	s_cbranch_execz .LBB0_2600
	global_load_dword v16, v[12:13], off
	s_branch .LBB0_2600
